# v68 + SwiGLU epilogue VALU trim: 16 redundant zero-init movs removed, 7 store addresses advanced incrementally (no 64-bit mad) in the three fp8 up-projection epilogues
# speedup vs baseline: 1.0025x; 1.0025x over previous
.LBB0_823:
.LBB0_825:
	v_exp_f32_e64 v18, -v156
	v_exp_f32_e64 v19, -v157
	v_pk_mul_f32 v[16:17], v[156:157], v[124:125]
	v_pk_mul_f32 v[10:11], v[162:163], v[130:131]
	v_exp_f32_e64 v14, -v160
	v_pk_add_f32 v[18:19], v[18:19], 1.0 op_sel_hi:[1,0]
	v_exp_f32_e64 v15, -v161
	v_rcp_f32_e32 v18, v18
	v_rcp_f32_e32 v19, v19
	v_pk_mul_f32 v[12:13], v[160:161], v[128:129]
	v_pk_add_f32 v[14:15], v[14:15], 1.0 op_sel_hi:[1,0]
	s_add_u32 s8, s81, 0xfffffe00
	v_pk_mul_f32 v[16:17], v[18:19], v[16:17]
	v_exp_f32_e64 v18, -v162
	v_exp_f32_e64 v19, -v163
	v_rcp_f32_e32 v14, v14
	v_rcp_f32_e32 v15, v15
	s_addc_u32 s9, s82, -1
	v_pk_add_f32 v[18:19], v[18:19], 1.0 op_sel_hi:[1,0]
	v_mov_b32_e32 v3, v1
	v_rcp_f32_e32 v18, v18
	v_rcp_f32_e32 v19, v19
	v_pk_mul_f32 v[12:13], v[14:15], v[12:13]
	v_pk_mul_f32 v[14:15], v[158:159], v[126:127]
	v_med3_f32 v7, v12, s13, v250
	v_pk_mul_f32 v[10:11], v[18:19], v[10:11]
	v_exp_f32_e64 v18, -v158
	v_exp_f32_e64 v19, -v159
	v_med3_f32 v12, v13, s13, v250
	v_med3_f32 v13, v10, s13, v250
	v_pk_add_f32 v[18:19], v[18:19], 1.0 op_sel_hi:[1,0]
	v_cvt_pk_fp8_f32 v10, v7, v12
	v_rcp_f32_e32 v18, v18
	v_rcp_f32_e32 v19, v19
	v_med3_f32 v11, v11, s13, v250
	v_cvt_pk_fp8_f32 v10, v13, v11 op_sel:[0,0,1]
	v_med3_f32 v7, v16, s13, v250
	v_pk_mul_f32 v[14:15], v[18:19], v[14:15]
	v_exp_f32_e64 v18, -v148
	v_exp_f32_e64 v19, -v149
	v_med3_f32 v12, v17, s13, v250
	v_pk_mul_f32 v[16:17], v[148:149], v[116:117]
	v_pk_add_f32 v[18:19], v[18:19], 1.0 op_sel_hi:[1,0]
	v_cvt_pk_fp8_f32 v11, v7, v12
	v_rcp_f32_e32 v18, v18
	v_rcp_f32_e32 v19, v19
	v_mov_b32_e32 v2, v165
	s_lshl_b32 s14, s49, 8
	s_lshl_b32 s30, s48, 7
	v_pk_mul_f32 v[16:17], v[18:19], v[16:17]
	v_exp_f32_e64 v18, -v154
	v_exp_f32_e64 v19, -v155
	v_readlane_b32 s26, v253, 26
	v_med3_f32 v13, v14, s13, v250
	v_med3_f32 v14, v15, s13, v250
	s_or_b32 s30, s30, s74
	s_add_i32 s14, s14, s73
	v_readlane_b32 s27, v253, 27
	v_cvt_pk_fp8_f32 v11, v13, v14 op_sel:[0,0,1]
	v_pk_add_f32 v[18:19], v[18:19], 1.0 op_sel_hi:[1,0]
	v_lshl_add_u32 v2, v2, 3, s30
	v_add_u32_e32 v6, s14, v3
	v_mov_b64_e32 v[4:5], s[26:27]
	s_movk_i32 s14, 0xe00
	v_rcp_f32_e32 v18, v18
	v_rcp_f32_e32 v19, v19
	v_ashrrev_i32_e32 v3, 31, v2
	v_mad_i64_i32 v[8:9], s[30:31], v6, s14, v[4:5]
	v_lshl_add_u64 v[8:9], v[8:9], 0, v[2:3]
	global_store_dwordx2 v[8:9], v[10:11], off
	v_mov_b32_e32 v180, 0xe000
	v_mov_b32_e32 v181, v35
	v_mov_b64_e32 v[182:183], v[8:9]
	v_lshl_add_u64 v[182:183], v[182:183], 0, v[180:181]
	v_pk_mul_f32 v[10:11], v[154:155], v[122:123]
	v_exp_f32_e64 v14, -v152
	v_exp_f32_e64 v15, -v153
	v_pk_mul_f32 v[10:11], v[18:19], v[10:11]
	v_exp_f32_e64 v18, -v150
	v_exp_f32_e64 v19, -v151
	v_pk_add_f32 v[14:15], v[14:15], 1.0 op_sel_hi:[1,0]
	v_pk_mul_f32 v[12:13], v[152:153], v[120:121]
	v_rcp_f32_e32 v14, v14
	v_rcp_f32_e32 v15, v15
	v_pk_add_f32 v[18:19], v[18:19], 1.0 op_sel_hi:[1,0]
	v_rcp_f32_e32 v18, v18
	v_rcp_f32_e32 v19, v19
	v_pk_mul_f32 v[12:13], v[14:15], v[12:13]
	v_pk_mul_f32 v[14:15], v[150:151], v[118:119]
	v_pk_mul_f32 v[14:15], v[18:19], v[14:15]
	v_exp_f32_e64 v18, -v140
	v_exp_f32_e64 v19, -v141
	v_med3_f32 v7, v12, s13, v250
	v_med3_f32 v12, v13, s13, v250
	v_med3_f32 v13, v10, s13, v250
	v_cvt_pk_fp8_f32 v10, v7, v12
	v_pk_add_f32 v[18:19], v[18:19], 1.0 op_sel_hi:[1,0]
	v_med3_f32 v11, v11, s13, v250
	v_rcp_f32_e32 v18, v18
	v_rcp_f32_e32 v19, v19
	v_cvt_pk_fp8_f32 v10, v13, v11 op_sel:[0,0,1]
	v_med3_f32 v7, v16, s13, v250
	v_med3_f32 v12, v17, s13, v250
	v_pk_mul_f32 v[16:17], v[140:141], v[108:109]
	v_cvt_pk_fp8_f32 v11, v7, v12
	v_pk_mul_f32 v[16:17], v[18:19], v[16:17]
	v_exp_f32_e64 v18, -v146
	v_exp_f32_e64 v19, -v147
	v_med3_f32 v13, v14, s13, v250
	v_med3_f32 v14, v15, s13, v250
	v_cvt_pk_fp8_f32 v11, v13, v14 op_sel:[0,0,1]
	v_pk_add_f32 v[18:19], v[18:19], 1.0 op_sel_hi:[1,0]
	v_rcp_f32_e32 v18, v18
	v_rcp_f32_e32 v19, v19
	global_store_dwordx2 v[182:183], v[10:11], off
	v_lshl_add_u64 v[182:183], v[182:183], 0, v[180:181]
	s_and_b64 vcc, exec, s[16:17]
	s_cbranch_vccz .Lepi_nobar_0
	s_barrier
.Lepi_nobar_0:
	v_pk_mul_f32 v[10:11], v[146:147], v[114:115]
	v_exp_f32_e64 v14, -v144
	v_exp_f32_e64 v15, -v145
	v_pk_mul_f32 v[10:11], v[18:19], v[10:11]
	v_exp_f32_e64 v18, -v142
	v_exp_f32_e64 v19, -v143
	v_pk_add_f32 v[14:15], v[14:15], 1.0 op_sel_hi:[1,0]
	v_pk_mul_f32 v[12:13], v[144:145], v[112:113]
	v_rcp_f32_e32 v14, v14
	v_rcp_f32_e32 v15, v15
	v_pk_add_f32 v[18:19], v[18:19], 1.0 op_sel_hi:[1,0]
	v_rcp_f32_e32 v18, v18
	v_rcp_f32_e32 v19, v19
	v_pk_mul_f32 v[12:13], v[14:15], v[12:13]
	v_pk_mul_f32 v[14:15], v[142:143], v[110:111]
	v_pk_mul_f32 v[14:15], v[18:19], v[14:15]
	v_exp_f32_e64 v18, -v132
	v_exp_f32_e64 v19, -v133
	v_med3_f32 v7, v12, s13, v250
	v_med3_f32 v12, v13, s13, v250
	v_med3_f32 v13, v10, s13, v250
	v_cvt_pk_fp8_f32 v10, v7, v12
	v_pk_add_f32 v[18:19], v[18:19], 1.0 op_sel_hi:[1,0]
	v_med3_f32 v11, v11, s13, v250
	v_rcp_f32_e32 v18, v18
	v_rcp_f32_e32 v19, v19
	v_cvt_pk_fp8_f32 v10, v13, v11 op_sel:[0,0,1]
	v_med3_f32 v7, v16, s13, v250
	v_med3_f32 v12, v17, s13, v250
	v_pk_mul_f32 v[16:17], v[132:133], v[100:101]
	v_cvt_pk_fp8_f32 v11, v7, v12
	v_pk_mul_f32 v[16:17], v[18:19], v[16:17]
	v_exp_f32_e64 v18, -v138
	v_exp_f32_e64 v19, -v139
	v_med3_f32 v13, v14, s13, v250
	v_med3_f32 v14, v15, s13, v250
	v_cvt_pk_fp8_f32 v11, v13, v14 op_sel:[0,0,1]
	v_pk_add_f32 v[18:19], v[18:19], 1.0 op_sel_hi:[1,0]
	v_rcp_f32_e32 v18, v18
	v_rcp_f32_e32 v19, v19
	global_store_dwordx2 v[182:183], v[10:11], off
	v_lshl_add_u64 v[182:183], v[182:183], 0, v[180:181]
	v_pk_mul_f32 v[10:11], v[138:139], v[106:107]
	v_exp_f32_e64 v14, -v136
	v_exp_f32_e64 v15, -v137
	v_pk_mul_f32 v[10:11], v[18:19], v[10:11]
	v_exp_f32_e64 v18, -v134
	v_exp_f32_e64 v19, -v135
	v_pk_add_f32 v[14:15], v[14:15], 1.0 op_sel_hi:[1,0]
	v_pk_mul_f32 v[12:13], v[136:137], v[104:105]
	v_rcp_f32_e32 v14, v14
	v_rcp_f32_e32 v15, v15
	v_pk_add_f32 v[18:19], v[18:19], 1.0 op_sel_hi:[1,0]
	v_rcp_f32_e32 v18, v18
	v_rcp_f32_e32 v19, v19
	v_pk_mul_f32 v[12:13], v[14:15], v[12:13]
	v_pk_mul_f32 v[14:15], v[134:135], v[102:103]
	v_pk_mul_f32 v[14:15], v[18:19], v[14:15]
	v_exp_f32_e64 v18, -v92
	v_exp_f32_e64 v19, -v93
	v_med3_f32 v7, v12, s13, v250
	v_med3_f32 v12, v13, s13, v250
	v_med3_f32 v13, v10, s13, v250
	v_cvt_pk_fp8_f32 v10, v7, v12
	v_pk_add_f32 v[18:19], v[18:19], 1.0 op_sel_hi:[1,0]
	v_med3_f32 v11, v11, s13, v250
	v_rcp_f32_e32 v18, v18
	v_rcp_f32_e32 v19, v19
	v_cvt_pk_fp8_f32 v10, v13, v11 op_sel:[0,0,1]
	v_med3_f32 v7, v16, s13, v250
	v_med3_f32 v12, v17, s13, v250
	v_pk_mul_f32 v[16:17], v[92:93], v[60:61]
	v_cvt_pk_fp8_f32 v11, v7, v12
	v_pk_mul_f32 v[16:17], v[18:19], v[16:17]
	v_exp_f32_e64 v18, -v98
	v_exp_f32_e64 v19, -v99
	v_med3_f32 v13, v14, s13, v250
	v_med3_f32 v14, v15, s13, v250
	v_cvt_pk_fp8_f32 v11, v13, v14 op_sel:[0,0,1]
	v_pk_add_f32 v[18:19], v[18:19], 1.0 op_sel_hi:[1,0]
	v_rcp_f32_e32 v18, v18
	v_rcp_f32_e32 v19, v19
	global_store_dwordx2 v[182:183], v[10:11], off
	v_lshl_add_u64 v[182:183], v[180:181], 2, v[182:183]
	v_lshl_add_u64 v[182:183], v[182:183], 0, v[180:181]
	v_pk_mul_f32 v[10:11], v[98:99], v[66:67]
	v_exp_f32_e64 v14, -v96
	v_exp_f32_e64 v15, -v97
	v_pk_mul_f32 v[10:11], v[18:19], v[10:11]
	v_exp_f32_e64 v18, -v94
	v_exp_f32_e64 v19, -v95
	v_pk_add_f32 v[14:15], v[14:15], 1.0 op_sel_hi:[1,0]
	v_pk_mul_f32 v[12:13], v[96:97], v[64:65]
	v_rcp_f32_e32 v14, v14
	v_rcp_f32_e32 v15, v15
	v_pk_add_f32 v[18:19], v[18:19], 1.0 op_sel_hi:[1,0]
	v_rcp_f32_e32 v18, v18
	v_rcp_f32_e32 v19, v19
	v_pk_mul_f32 v[12:13], v[14:15], v[12:13]
	v_pk_mul_f32 v[14:15], v[94:95], v[62:63]
	v_pk_mul_f32 v[14:15], v[18:19], v[14:15]
	v_exp_f32_e64 v18, -v84
	v_exp_f32_e64 v19, -v85
	v_med3_f32 v7, v12, s13, v250
	v_med3_f32 v12, v13, s13, v250
	v_med3_f32 v13, v10, s13, v250
	v_cvt_pk_fp8_f32 v10, v7, v12
	v_pk_add_f32 v[18:19], v[18:19], 1.0 op_sel_hi:[1,0]
	v_med3_f32 v11, v11, s13, v250
	v_rcp_f32_e32 v18, v18
	v_rcp_f32_e32 v19, v19
	v_cvt_pk_fp8_f32 v10, v13, v11 op_sel:[0,0,1]
	v_med3_f32 v7, v16, s13, v250
	v_med3_f32 v12, v17, s13, v250
	v_pk_mul_f32 v[16:17], v[84:85], v[52:53]
	v_cvt_pk_fp8_f32 v11, v7, v12
	v_pk_mul_f32 v[16:17], v[18:19], v[16:17]
	v_exp_f32_e64 v18, -v90
	v_exp_f32_e64 v19, -v91
	v_med3_f32 v13, v14, s13, v250
	v_med3_f32 v14, v15, s13, v250
	v_cvt_pk_fp8_f32 v11, v13, v14 op_sel:[0,0,1]
	v_pk_add_f32 v[18:19], v[18:19], 1.0 op_sel_hi:[1,0]
	v_rcp_f32_e32 v18, v18
	v_rcp_f32_e32 v19, v19
	v_exp_f32_e64 v14, -v88
	v_exp_f32_e64 v15, -v89
	global_store_dwordx2 v[182:183], v[10:11], off
	v_lshl_add_u64 v[182:183], v[182:183], 0, v[180:181]
	v_pk_mul_f32 v[10:11], v[90:91], v[58:59]
	v_pk_mul_f32 v[12:13], v[88:89], v[56:57]
	v_pk_mul_f32 v[10:11], v[18:19], v[10:11]
	v_exp_f32_e64 v18, -v86
	v_exp_f32_e64 v19, -v87
	v_pk_add_f32 v[14:15], v[14:15], 1.0 op_sel_hi:[1,0]
	v_rcp_f32_e32 v14, v14
	v_rcp_f32_e32 v15, v15
	v_pk_add_f32 v[18:19], v[18:19], 1.0 op_sel_hi:[1,0]
	v_rcp_f32_e32 v18, v18
	v_rcp_f32_e32 v19, v19
	v_pk_mul_f32 v[12:13], v[14:15], v[12:13]
	v_pk_mul_f32 v[14:15], v[86:87], v[54:55]
	v_med3_f32 v7, v12, s13, v250
	v_med3_f32 v12, v13, s13, v250
	v_med3_f32 v13, v10, s13, v250
	v_pk_mul_f32 v[14:15], v[18:19], v[14:15]
	v_cvt_pk_fp8_f32 v10, v7, v12
	v_exp_f32_e64 v18, -v76
	v_exp_f32_e64 v19, -v77
	v_med3_f32 v11, v11, s13, v250
	v_cvt_pk_fp8_f32 v10, v13, v11 op_sel:[0,0,1]
	v_med3_f32 v7, v16, s13, v250
	v_med3_f32 v12, v17, s13, v250
	v_pk_add_f32 v[18:19], v[18:19], 1.0 op_sel_hi:[1,0]
	v_cvt_pk_fp8_f32 v11, v7, v12
	v_rcp_f32_e32 v18, v18
	v_rcp_f32_e32 v19, v19
	v_med3_f32 v13, v14, s13, v250
	v_med3_f32 v14, v15, s13, v250
	v_pk_mul_f32 v[16:17], v[76:77], v[44:45]
	v_cvt_pk_fp8_f32 v11, v13, v14 op_sel:[0,0,1]
	v_exp_f32_e64 v14, -v80
	v_exp_f32_e64 v15, -v81
	v_pk_mul_f32 v[16:17], v[18:19], v[16:17]
	v_exp_f32_e64 v18, -v82
	v_exp_f32_e64 v19, -v83
	v_pk_add_f32 v[14:15], v[14:15], 1.0 op_sel_hi:[1,0]
	v_rcp_f32_e32 v14, v14
	v_pk_add_f32 v[18:19], v[18:19], 1.0 op_sel_hi:[1,0]
	v_rcp_f32_e32 v15, v15
	v_rcp_f32_e32 v18, v18
	v_rcp_f32_e32 v19, v19
	global_store_dwordx2 v[182:183], v[10:11], off
	v_lshl_add_u64 v[182:183], v[182:183], 0, v[180:181]
	v_pk_mul_f32 v[10:11], v[82:83], v[50:51]
	v_pk_mul_f32 v[12:13], v[80:81], v[48:49]
	v_pk_mul_f32 v[12:13], v[14:15], v[12:13]
	v_pk_mul_f32 v[10:11], v[18:19], v[10:11]
	v_exp_f32_e64 v18, -v78
	v_exp_f32_e64 v19, -v79
	v_med3_f32 v7, v12, s13, v250
	v_med3_f32 v12, v13, s13, v250
	v_med3_f32 v13, v10, s13, v250
	v_cvt_pk_fp8_f32 v10, v7, v12
	v_pk_add_f32 v[18:19], v[18:19], 1.0 op_sel_hi:[1,0]
	v_med3_f32 v11, v11, s13, v250
	v_rcp_f32_e32 v18, v18
	v_rcp_f32_e32 v19, v19
	v_cvt_pk_fp8_f32 v10, v13, v11 op_sel:[0,0,1]
	v_med3_f32 v7, v16, s13, v250
	v_med3_f32 v12, v17, s13, v250
	v_cvt_pk_fp8_f32 v11, v7, v12
	v_pk_mul_f32 v[14:15], v[78:79], v[46:47]
	v_pk_mul_f32 v[14:15], v[18:19], v[14:15]
	v_med3_f32 v13, v14, s13, v250
	v_med3_f32 v14, v15, s13, v250
	v_cvt_pk_fp8_f32 v11, v13, v14 op_sel:[0,0,1]
	v_exp_f32_e64 v14, -v68
	v_exp_f32_e64 v15, -v69
	v_pk_mul_f32 v[12:13], v[68:69], v[36:37]
	global_store_dwordx2 v[182:183], v[10:11], off
	v_lshl_add_u64 v[182:183], v[182:183], 0, v[180:181]
	v_exp_f32_e64 v10, -v72
	v_pk_add_f32 v[14:15], v[14:15], 1.0 op_sel_hi:[1,0]
	v_exp_f32_e64 v11, -v73
	v_rcp_f32_e32 v14, v14
	v_rcp_f32_e32 v15, v15
	v_pk_add_f32 v[10:11], v[10:11], 1.0 op_sel_hi:[1,0]
	v_pk_mul_f32 v[12:13], v[14:15], v[12:13]
	v_exp_f32_e64 v14, -v74
	v_exp_f32_e64 v15, -v75
	v_rcp_f32_e32 v10, v10
	v_rcp_f32_e32 v11, v11
	v_pk_mul_f32 v[6:7], v[74:75], v[42:43]
	v_pk_add_f32 v[14:15], v[14:15], 1.0 op_sel_hi:[1,0]
	v_pk_mul_f32 v[8:9], v[72:73], v[40:41]
	v_rcp_f32_e32 v14, v14
	v_rcp_f32_e32 v15, v15
	v_pk_mul_f32 v[8:9], v[10:11], v[8:9]
	v_med3_f32 v5, v8, s13, v250
	v_pk_mul_f32 v[6:7], v[14:15], v[6:7]
	v_exp_f32_e64 v14, -v70
	v_exp_f32_e64 v15, -v71
	v_med3_f32 v8, v9, s13, v250
	v_cvt_pk_fp8_f32 v4, v5, v8
	v_pk_add_f32 v[14:15], v[14:15], 1.0 op_sel_hi:[1,0]
	v_med3_f32 v6, v6, s13, v250
	v_rcp_f32_e32 v14, v14
	v_rcp_f32_e32 v15, v15
	v_med3_f32 v7, v7, s13, v250
	v_cvt_pk_fp8_f32 v4, v6, v7 op_sel:[0,0,1]
	v_med3_f32 v6, v12, s13, v250
	v_med3_f32 v7, v13, s13, v250
	v_cvt_pk_fp8_f32 v5, v6, v7
	v_pk_mul_f32 v[10:11], v[70:71], v[38:39]
	s_and_b64 vcc, exec, s[6:7]
	v_pk_mul_f32 v[10:11], v[14:15], v[10:11]
	s_mov_b64 s[84:85], s[24:25]
	v_med3_f32 v8, v10, s13, v250
	v_med3_f32 v9, v11, s13, v250
	v_cvt_pk_fp8_f32 v5, v8, v9 op_sel:[0,0,1]
	global_store_dwordx2 v[182:183], v[4:5], off
	s_cbranch_vccnz .LBB0_828
	s_andn2_b64 vcc, exec, s[10:11]
	s_cbranch_vccnz .LBB0_810
	s_barrier
	s_branch .LBB0_810

.LBB0_957:
.LBB0_959:
	v_exp_f32_e64 v18, -v156
	v_exp_f32_e64 v19, -v157
	v_pk_mul_f32 v[16:17], v[156:157], v[124:125]
	v_pk_mul_f32 v[10:11], v[162:163], v[130:131]
	v_exp_f32_e64 v14, -v160
	v_pk_add_f32 v[18:19], v[18:19], 1.0 op_sel_hi:[1,0]
	v_exp_f32_e64 v15, -v161
	v_rcp_f32_e32 v18, v18
	v_rcp_f32_e32 v19, v19
	v_pk_mul_f32 v[12:13], v[160:161], v[128:129]
	v_pk_add_f32 v[14:15], v[14:15], 1.0 op_sel_hi:[1,0]
	s_add_u32 s30, s95, 0xfffffe00
	v_pk_mul_f32 v[16:17], v[18:19], v[16:17]
	v_exp_f32_e64 v18, -v162
	v_exp_f32_e64 v19, -v163
	v_rcp_f32_e32 v14, v14
	v_rcp_f32_e32 v15, v15
	s_addc_u32 s31, s96, -1
	v_pk_add_f32 v[18:19], v[18:19], 1.0 op_sel_hi:[1,0]
	v_mov_b32_e32 v3, v1
	v_rcp_f32_e32 v18, v18
	v_rcp_f32_e32 v19, v19
	v_pk_mul_f32 v[12:13], v[14:15], v[12:13]
	v_pk_mul_f32 v[14:15], v[158:159], v[126:127]
	v_med3_f32 v7, v12, s13, v250
	v_pk_mul_f32 v[10:11], v[18:19], v[10:11]
	v_exp_f32_e64 v18, -v158
	v_exp_f32_e64 v19, -v159
	v_med3_f32 v12, v13, s13, v250
	v_med3_f32 v13, v10, s13, v250
	v_pk_add_f32 v[18:19], v[18:19], 1.0 op_sel_hi:[1,0]
	v_cvt_pk_fp8_f32 v10, v7, v12
	v_rcp_f32_e32 v18, v18
	v_rcp_f32_e32 v19, v19
	v_med3_f32 v11, v11, s13, v250
	v_cvt_pk_fp8_f32 v10, v13, v11 op_sel:[0,0,1]
	v_med3_f32 v7, v16, s13, v250
	v_pk_mul_f32 v[14:15], v[18:19], v[14:15]
	v_exp_f32_e64 v18, -v148
	v_exp_f32_e64 v19, -v149
	v_med3_f32 v12, v17, s13, v250
	v_pk_mul_f32 v[16:17], v[148:149], v[116:117]
	v_pk_add_f32 v[18:19], v[18:19], 1.0 op_sel_hi:[1,0]
	v_cvt_pk_fp8_f32 v11, v7, v12
	v_rcp_f32_e32 v18, v18
	v_rcp_f32_e32 v19, v19
	v_mov_b32_e32 v2, v165
	s_lshl_b32 s14, s77, 8
	s_lshl_b32 s46, s76, 7
	v_pk_mul_f32 v[16:17], v[18:19], v[16:17]
	v_exp_f32_e64 v18, -v154
	v_exp_f32_e64 v19, -v155
	v_med3_f32 v13, v14, s13, v250
	v_med3_f32 v14, v15, s13, v250
	s_or_b32 s46, s46, s89
	s_add_i32 s14, s14, s87
	v_cvt_pk_fp8_f32 v11, v13, v14 op_sel:[0,0,1]
	v_pk_add_f32 v[18:19], v[18:19], 1.0 op_sel_hi:[1,0]
	v_lshl_add_u32 v2, v2, 3, s46
	v_add_u32_e32 v6, s14, v3
	v_mov_b64_e32 v[4:5], s[22:23]
	s_movk_i32 s14, 0xe00
	v_rcp_f32_e32 v18, v18
	v_rcp_f32_e32 v19, v19
	v_ashrrev_i32_e32 v3, 31, v2
	v_mad_i64_i32 v[8:9], s[46:47], v6, s14, v[4:5]
	v_lshl_add_u64 v[8:9], v[8:9], 0, v[2:3]
	global_store_dwordx2 v[8:9], v[10:11], off
	v_mov_b32_e32 v230, 0xe000
	v_mov_b32_e32 v231, v35
	v_mov_b64_e32 v[232:233], v[8:9]
	v_lshl_add_u64 v[232:233], v[232:233], 0, v[230:231]
	v_pk_mul_f32 v[10:11], v[154:155], v[122:123]
	v_exp_f32_e64 v14, -v152
	v_exp_f32_e64 v15, -v153
	v_pk_mul_f32 v[10:11], v[18:19], v[10:11]
	v_exp_f32_e64 v18, -v150
	v_exp_f32_e64 v19, -v151
	v_pk_add_f32 v[14:15], v[14:15], 1.0 op_sel_hi:[1,0]
	v_pk_mul_f32 v[12:13], v[152:153], v[120:121]
	v_rcp_f32_e32 v14, v14
	v_rcp_f32_e32 v15, v15
	v_pk_add_f32 v[18:19], v[18:19], 1.0 op_sel_hi:[1,0]
	v_rcp_f32_e32 v18, v18
	v_rcp_f32_e32 v19, v19
	v_pk_mul_f32 v[12:13], v[14:15], v[12:13]
	v_pk_mul_f32 v[14:15], v[150:151], v[118:119]
	v_pk_mul_f32 v[14:15], v[18:19], v[14:15]
	v_exp_f32_e64 v18, -v140
	v_exp_f32_e64 v19, -v141
	v_med3_f32 v7, v12, s13, v250
	v_med3_f32 v12, v13, s13, v250
	v_med3_f32 v13, v10, s13, v250
	v_cvt_pk_fp8_f32 v10, v7, v12
	v_pk_add_f32 v[18:19], v[18:19], 1.0 op_sel_hi:[1,0]
	v_med3_f32 v11, v11, s13, v250
	v_rcp_f32_e32 v18, v18
	v_rcp_f32_e32 v19, v19
	v_cvt_pk_fp8_f32 v10, v13, v11 op_sel:[0,0,1]
	v_med3_f32 v7, v16, s13, v250
	v_med3_f32 v12, v17, s13, v250
	v_pk_mul_f32 v[16:17], v[140:141], v[108:109]
	v_cvt_pk_fp8_f32 v11, v7, v12
	v_pk_mul_f32 v[16:17], v[18:19], v[16:17]
	v_exp_f32_e64 v18, -v146
	v_exp_f32_e64 v19, -v147
	v_med3_f32 v13, v14, s13, v250
	v_med3_f32 v14, v15, s13, v250
	v_cvt_pk_fp8_f32 v11, v13, v14 op_sel:[0,0,1]
	v_pk_add_f32 v[18:19], v[18:19], 1.0 op_sel_hi:[1,0]
	v_rcp_f32_e32 v18, v18
	v_rcp_f32_e32 v19, v19
	global_store_dwordx2 v[232:233], v[10:11], off
	v_lshl_add_u64 v[232:233], v[232:233], 0, v[230:231]
	s_and_b64 vcc, exec, s[36:37]
	s_cbranch_vccz .Lepi_nobar_1
	s_barrier
.Lepi_nobar_1:
	v_pk_mul_f32 v[10:11], v[146:147], v[114:115]
	v_exp_f32_e64 v14, -v144
	v_exp_f32_e64 v15, -v145
	v_pk_mul_f32 v[10:11], v[18:19], v[10:11]
	v_exp_f32_e64 v18, -v142
	v_exp_f32_e64 v19, -v143
	v_pk_add_f32 v[14:15], v[14:15], 1.0 op_sel_hi:[1,0]
	v_pk_mul_f32 v[12:13], v[144:145], v[112:113]
	v_rcp_f32_e32 v14, v14
	v_rcp_f32_e32 v15, v15
	v_pk_add_f32 v[18:19], v[18:19], 1.0 op_sel_hi:[1,0]
	v_rcp_f32_e32 v18, v18
	v_rcp_f32_e32 v19, v19
	v_pk_mul_f32 v[12:13], v[14:15], v[12:13]
	v_pk_mul_f32 v[14:15], v[142:143], v[110:111]
	v_pk_mul_f32 v[14:15], v[18:19], v[14:15]
	v_exp_f32_e64 v18, -v132
	v_exp_f32_e64 v19, -v133
	v_med3_f32 v7, v12, s13, v250
	v_med3_f32 v12, v13, s13, v250
	v_med3_f32 v13, v10, s13, v250
	v_cvt_pk_fp8_f32 v10, v7, v12
	v_pk_add_f32 v[18:19], v[18:19], 1.0 op_sel_hi:[1,0]
	v_med3_f32 v11, v11, s13, v250
	v_rcp_f32_e32 v18, v18
	v_rcp_f32_e32 v19, v19
	v_cvt_pk_fp8_f32 v10, v13, v11 op_sel:[0,0,1]
	v_med3_f32 v7, v16, s13, v250
	v_med3_f32 v12, v17, s13, v250
	v_pk_mul_f32 v[16:17], v[132:133], v[100:101]
	v_cvt_pk_fp8_f32 v11, v7, v12
	v_pk_mul_f32 v[16:17], v[18:19], v[16:17]
	v_exp_f32_e64 v18, -v138
	v_exp_f32_e64 v19, -v139
	v_med3_f32 v13, v14, s13, v250
	v_med3_f32 v14, v15, s13, v250
	v_cvt_pk_fp8_f32 v11, v13, v14 op_sel:[0,0,1]
	v_pk_add_f32 v[18:19], v[18:19], 1.0 op_sel_hi:[1,0]
	v_rcp_f32_e32 v18, v18
	v_rcp_f32_e32 v19, v19
	global_store_dwordx2 v[232:233], v[10:11], off
	v_lshl_add_u64 v[232:233], v[232:233], 0, v[230:231]
	v_pk_mul_f32 v[10:11], v[138:139], v[106:107]
	v_exp_f32_e64 v14, -v136
	v_exp_f32_e64 v15, -v137
	v_pk_mul_f32 v[10:11], v[18:19], v[10:11]
	v_exp_f32_e64 v18, -v134
	v_exp_f32_e64 v19, -v135
	v_pk_add_f32 v[14:15], v[14:15], 1.0 op_sel_hi:[1,0]
	v_pk_mul_f32 v[12:13], v[136:137], v[104:105]
	v_rcp_f32_e32 v14, v14
	v_rcp_f32_e32 v15, v15
	v_pk_add_f32 v[18:19], v[18:19], 1.0 op_sel_hi:[1,0]
	v_rcp_f32_e32 v18, v18
	v_rcp_f32_e32 v19, v19
	v_pk_mul_f32 v[12:13], v[14:15], v[12:13]
	v_pk_mul_f32 v[14:15], v[134:135], v[102:103]
	v_pk_mul_f32 v[14:15], v[18:19], v[14:15]
	v_exp_f32_e64 v18, -v92
	v_exp_f32_e64 v19, -v93
	v_med3_f32 v7, v12, s13, v250
	v_med3_f32 v12, v13, s13, v250
	v_med3_f32 v13, v10, s13, v250
	v_cvt_pk_fp8_f32 v10, v7, v12
	v_pk_add_f32 v[18:19], v[18:19], 1.0 op_sel_hi:[1,0]
	v_med3_f32 v11, v11, s13, v250
	v_rcp_f32_e32 v18, v18
	v_rcp_f32_e32 v19, v19
	v_cvt_pk_fp8_f32 v10, v13, v11 op_sel:[0,0,1]
	v_med3_f32 v7, v16, s13, v250
	v_med3_f32 v12, v17, s13, v250
	v_pk_mul_f32 v[16:17], v[92:93], v[60:61]
	v_cvt_pk_fp8_f32 v11, v7, v12
	v_pk_mul_f32 v[16:17], v[18:19], v[16:17]
	v_exp_f32_e64 v18, -v98
	v_exp_f32_e64 v19, -v99
	v_med3_f32 v13, v14, s13, v250
	v_med3_f32 v14, v15, s13, v250
	v_cvt_pk_fp8_f32 v11, v13, v14 op_sel:[0,0,1]
	v_pk_add_f32 v[18:19], v[18:19], 1.0 op_sel_hi:[1,0]
	v_rcp_f32_e32 v18, v18
	v_rcp_f32_e32 v19, v19
	global_store_dwordx2 v[232:233], v[10:11], off
	v_lshl_add_u64 v[232:233], v[230:231], 2, v[232:233]
	v_lshl_add_u64 v[232:233], v[232:233], 0, v[230:231]
	v_pk_mul_f32 v[10:11], v[98:99], v[66:67]
	v_exp_f32_e64 v14, -v96
	v_exp_f32_e64 v15, -v97
	v_pk_mul_f32 v[10:11], v[18:19], v[10:11]
	v_exp_f32_e64 v18, -v94
	v_exp_f32_e64 v19, -v95
	v_pk_add_f32 v[14:15], v[14:15], 1.0 op_sel_hi:[1,0]
	v_pk_mul_f32 v[12:13], v[96:97], v[64:65]
	v_rcp_f32_e32 v14, v14
	v_rcp_f32_e32 v15, v15
	v_pk_add_f32 v[18:19], v[18:19], 1.0 op_sel_hi:[1,0]
	v_rcp_f32_e32 v18, v18
	v_rcp_f32_e32 v19, v19
	v_pk_mul_f32 v[12:13], v[14:15], v[12:13]
	v_pk_mul_f32 v[14:15], v[94:95], v[62:63]
	v_pk_mul_f32 v[14:15], v[18:19], v[14:15]
	v_exp_f32_e64 v18, -v84
	v_exp_f32_e64 v19, -v85
	v_med3_f32 v7, v12, s13, v250
	v_med3_f32 v12, v13, s13, v250
	v_med3_f32 v13, v10, s13, v250
	v_cvt_pk_fp8_f32 v10, v7, v12
	v_pk_add_f32 v[18:19], v[18:19], 1.0 op_sel_hi:[1,0]
	v_med3_f32 v11, v11, s13, v250
	v_rcp_f32_e32 v18, v18
	v_rcp_f32_e32 v19, v19
	v_cvt_pk_fp8_f32 v10, v13, v11 op_sel:[0,0,1]
	v_med3_f32 v7, v16, s13, v250
	v_med3_f32 v12, v17, s13, v250
	v_pk_mul_f32 v[16:17], v[84:85], v[52:53]
	v_cvt_pk_fp8_f32 v11, v7, v12
	v_pk_mul_f32 v[16:17], v[18:19], v[16:17]
	v_exp_f32_e64 v18, -v90
	v_exp_f32_e64 v19, -v91
	v_med3_f32 v13, v14, s13, v250
	v_med3_f32 v14, v15, s13, v250
	v_cvt_pk_fp8_f32 v11, v13, v14 op_sel:[0,0,1]
	v_pk_add_f32 v[18:19], v[18:19], 1.0 op_sel_hi:[1,0]
	v_rcp_f32_e32 v18, v18
	v_rcp_f32_e32 v19, v19
	v_exp_f32_e64 v14, -v88
	v_exp_f32_e64 v15, -v89
	global_store_dwordx2 v[232:233], v[10:11], off
	v_lshl_add_u64 v[232:233], v[232:233], 0, v[230:231]
	v_pk_mul_f32 v[10:11], v[90:91], v[58:59]
	v_pk_mul_f32 v[12:13], v[88:89], v[56:57]
	v_pk_mul_f32 v[10:11], v[18:19], v[10:11]
	v_exp_f32_e64 v18, -v86
	v_exp_f32_e64 v19, -v87
	v_pk_add_f32 v[14:15], v[14:15], 1.0 op_sel_hi:[1,0]
	v_rcp_f32_e32 v14, v14
	v_rcp_f32_e32 v15, v15
	v_pk_add_f32 v[18:19], v[18:19], 1.0 op_sel_hi:[1,0]
	v_rcp_f32_e32 v18, v18
	v_rcp_f32_e32 v19, v19
	v_pk_mul_f32 v[12:13], v[14:15], v[12:13]
	v_pk_mul_f32 v[14:15], v[86:87], v[54:55]
	v_med3_f32 v7, v12, s13, v250
	v_med3_f32 v12, v13, s13, v250
	v_med3_f32 v13, v10, s13, v250
	v_pk_mul_f32 v[14:15], v[18:19], v[14:15]
	v_cvt_pk_fp8_f32 v10, v7, v12
	v_exp_f32_e64 v18, -v76
	v_exp_f32_e64 v19, -v77
	v_med3_f32 v11, v11, s13, v250
	v_cvt_pk_fp8_f32 v10, v13, v11 op_sel:[0,0,1]
	v_med3_f32 v7, v16, s13, v250
	v_med3_f32 v12, v17, s13, v250
	v_pk_add_f32 v[18:19], v[18:19], 1.0 op_sel_hi:[1,0]
	v_cvt_pk_fp8_f32 v11, v7, v12
	v_rcp_f32_e32 v18, v18
	v_rcp_f32_e32 v19, v19
	v_med3_f32 v13, v14, s13, v250
	v_med3_f32 v14, v15, s13, v250
	v_pk_mul_f32 v[16:17], v[76:77], v[44:45]
	v_cvt_pk_fp8_f32 v11, v13, v14 op_sel:[0,0,1]
	v_exp_f32_e64 v14, -v80
	v_exp_f32_e64 v15, -v81
	v_pk_mul_f32 v[16:17], v[18:19], v[16:17]
	v_exp_f32_e64 v18, -v82
	v_exp_f32_e64 v19, -v83
	v_pk_add_f32 v[14:15], v[14:15], 1.0 op_sel_hi:[1,0]
	v_rcp_f32_e32 v14, v14
	v_pk_add_f32 v[18:19], v[18:19], 1.0 op_sel_hi:[1,0]
	v_rcp_f32_e32 v15, v15
	v_rcp_f32_e32 v18, v18
	v_rcp_f32_e32 v19, v19
	global_store_dwordx2 v[232:233], v[10:11], off
	v_lshl_add_u64 v[232:233], v[232:233], 0, v[230:231]
	v_pk_mul_f32 v[10:11], v[82:83], v[50:51]
	v_pk_mul_f32 v[12:13], v[80:81], v[48:49]
	v_pk_mul_f32 v[12:13], v[14:15], v[12:13]
	v_pk_mul_f32 v[10:11], v[18:19], v[10:11]
	v_exp_f32_e64 v18, -v78
	v_exp_f32_e64 v19, -v79
	v_med3_f32 v7, v12, s13, v250
	v_med3_f32 v12, v13, s13, v250
	v_med3_f32 v13, v10, s13, v250
	v_cvt_pk_fp8_f32 v10, v7, v12
	v_pk_add_f32 v[18:19], v[18:19], 1.0 op_sel_hi:[1,0]
	v_med3_f32 v11, v11, s13, v250
	v_rcp_f32_e32 v18, v18
	v_rcp_f32_e32 v19, v19
	v_cvt_pk_fp8_f32 v10, v13, v11 op_sel:[0,0,1]
	v_med3_f32 v7, v16, s13, v250
	v_med3_f32 v12, v17, s13, v250
	v_cvt_pk_fp8_f32 v11, v7, v12
	v_pk_mul_f32 v[14:15], v[78:79], v[46:47]
	v_pk_mul_f32 v[14:15], v[18:19], v[14:15]
	v_med3_f32 v13, v14, s13, v250
	v_med3_f32 v14, v15, s13, v250
	v_cvt_pk_fp8_f32 v11, v13, v14 op_sel:[0,0,1]
	v_exp_f32_e64 v14, -v68
	v_exp_f32_e64 v15, -v69
	v_pk_mul_f32 v[12:13], v[68:69], v[36:37]
	global_store_dwordx2 v[232:233], v[10:11], off
	v_lshl_add_u64 v[232:233], v[232:233], 0, v[230:231]
	v_exp_f32_e64 v10, -v72
	v_pk_add_f32 v[14:15], v[14:15], 1.0 op_sel_hi:[1,0]
	v_exp_f32_e64 v11, -v73
	v_rcp_f32_e32 v14, v14
	v_rcp_f32_e32 v15, v15
	v_pk_add_f32 v[10:11], v[10:11], 1.0 op_sel_hi:[1,0]
	v_pk_mul_f32 v[12:13], v[14:15], v[12:13]
	v_exp_f32_e64 v14, -v74
	v_exp_f32_e64 v15, -v75
	v_rcp_f32_e32 v10, v10
	v_rcp_f32_e32 v11, v11
	v_pk_mul_f32 v[6:7], v[74:75], v[42:43]
	v_pk_add_f32 v[14:15], v[14:15], 1.0 op_sel_hi:[1,0]
	v_pk_mul_f32 v[8:9], v[72:73], v[40:41]
	v_rcp_f32_e32 v14, v14
	v_rcp_f32_e32 v15, v15
	v_pk_mul_f32 v[8:9], v[10:11], v[8:9]
	v_med3_f32 v5, v8, s13, v250
	v_pk_mul_f32 v[6:7], v[14:15], v[6:7]
	v_exp_f32_e64 v14, -v70
	v_exp_f32_e64 v15, -v71
	v_med3_f32 v8, v9, s13, v250
	v_cvt_pk_fp8_f32 v4, v5, v8
	v_pk_add_f32 v[14:15], v[14:15], 1.0 op_sel_hi:[1,0]
	v_med3_f32 v6, v6, s13, v250
	v_rcp_f32_e32 v14, v14
	v_rcp_f32_e32 v15, v15
	v_med3_f32 v7, v7, s13, v250
	v_cvt_pk_fp8_f32 v4, v6, v7 op_sel:[0,0,1]
	v_med3_f32 v6, v12, s13, v250
	v_med3_f32 v7, v13, s13, v250
	v_cvt_pk_fp8_f32 v5, v6, v7
	v_pk_mul_f32 v[10:11], v[70:71], v[38:39]
	s_andn2_b64 vcc, exec, s[44:45]
	v_pk_mul_f32 v[10:11], v[14:15], v[10:11]
	s_nop 0
	v_med3_f32 v8, v10, s13, v250
	v_med3_f32 v9, v11, s13, v250
	v_cvt_pk_fp8_f32 v5, v8, v9 op_sel:[0,0,1]
	global_store_dwordx2 v[232:233], v[4:5], off
	s_cbranch_vccnz .LBB0_962
	v_readlane_b32 s96, v254, 55
	s_andn2_b64 vcc, exec, s[6:7]
	v_readlane_b32 s95, v254, 48
	v_readlane_b32 s97, v254, 56
	s_cbranch_vccnz .LBB0_935
	s_barrier
	s_branch .LBB0_935

.LBB0_1090:
	v_exp_f32_e64 v18, -v156
	v_exp_f32_e64 v19, -v157
	v_pk_mul_f32 v[16:17], v[156:157], v[124:125]
	v_pk_mul_f32 v[10:11], v[162:163], v[130:131]
	v_exp_f32_e64 v14, -v160
	v_pk_add_f32 v[18:19], v[18:19], 1.0 op_sel_hi:[1,0]
	v_exp_f32_e64 v15, -v161
	v_rcp_f32_e32 v18, v18
	v_rcp_f32_e32 v19, v19
	v_pk_mul_f32 v[12:13], v[160:161], v[128:129]
	v_pk_add_f32 v[14:15], v[14:15], 1.0 op_sel_hi:[1,0]
	v_mov_b32_e32 v3, v1
	v_pk_mul_f32 v[16:17], v[18:19], v[16:17]
	v_exp_f32_e64 v18, -v162
	v_exp_f32_e64 v19, -v163
	v_rcp_f32_e32 v14, v14
	v_rcp_f32_e32 v15, v15
	v_mov_b32_e32 v2, v189
	v_pk_add_f32 v[18:19], v[18:19], 1.0 op_sel_hi:[1,0]
	s_lshl_b32 s22, s52, 7
	v_rcp_f32_e32 v18, v18
	v_rcp_f32_e32 v19, v19
	v_pk_mul_f32 v[12:13], v[14:15], v[12:13]
	v_pk_mul_f32 v[14:15], v[158:159], v[126:127]
	v_med3_f32 v7, v12, s13, v250
	v_pk_mul_f32 v[10:11], v[18:19], v[10:11]
	v_exp_f32_e64 v18, -v158
	v_exp_f32_e64 v19, -v159
	v_med3_f32 v12, v13, s13, v250
	v_med3_f32 v13, v10, s13, v250
	v_pk_add_f32 v[18:19], v[18:19], 1.0 op_sel_hi:[1,0]
	v_cvt_pk_fp8_f32 v10, v7, v12
	v_rcp_f32_e32 v18, v18
	v_rcp_f32_e32 v19, v19
	v_med3_f32 v11, v11, s13, v250
	v_cvt_pk_fp8_f32 v10, v13, v11 op_sel:[0,0,1]
	v_med3_f32 v7, v16, s13, v250
	v_pk_mul_f32 v[14:15], v[18:19], v[14:15]
	v_exp_f32_e64 v18, -v148
	v_exp_f32_e64 v19, -v149
	v_med3_f32 v12, v17, s13, v250
	v_pk_mul_f32 v[16:17], v[148:149], v[116:117]
	v_pk_add_f32 v[18:19], v[18:19], 1.0 op_sel_hi:[1,0]
	v_cvt_pk_fp8_f32 v11, v7, v12
	v_rcp_f32_e32 v18, v18
	v_rcp_f32_e32 v19, v19
	s_or_b32 s22, s22, s46
	v_pk_mul_f32 v[16:17], v[18:19], v[16:17]
	v_exp_f32_e64 v18, -v154
	v_exp_f32_e64 v19, -v155
	s_lshl_b32 s14, s53, 8
	v_lshl_add_u32 v2, v2, 3, s22
	v_readlane_b32 s22, v254, 4
	v_med3_f32 v13, v14, s13, v250
	v_med3_f32 v14, v15, s13, v250
	s_add_i32 s14, s14, s45
	v_readlane_b32 s23, v254, 5
	v_cvt_pk_fp8_f32 v11, v13, v14 op_sel:[0,0,1]
	v_pk_add_f32 v[18:19], v[18:19], 1.0 op_sel_hi:[1,0]
	v_add_u32_e32 v6, s14, v3
	v_mov_b64_e32 v[4:5], s[22:23]
	s_movk_i32 s14, 0xb00
	v_rcp_f32_e32 v18, v18
	v_rcp_f32_e32 v19, v19
	v_ashrrev_i32_e32 v3, 31, v2
	v_mad_i64_i32 v[8:9], s[22:23], v6, s14, v[4:5]
	v_lshl_add_u64 v[8:9], v[8:9], 0, v[2:3]
	global_store_dwordx2 v[8:9], v[10:11], off
	v_mov_b32_e32 v180, 0xb000
	v_mov_b32_e32 v181, v35
	v_mov_b64_e32 v[182:183], v[8:9]
	v_lshl_add_u64 v[182:183], v[182:183], 0, v[180:181]
	v_pk_mul_f32 v[10:11], v[154:155], v[122:123]
	v_exp_f32_e64 v14, -v152
	v_exp_f32_e64 v15, -v153
	v_pk_mul_f32 v[10:11], v[18:19], v[10:11]
	v_exp_f32_e64 v18, -v150
	v_exp_f32_e64 v19, -v151
	v_pk_add_f32 v[14:15], v[14:15], 1.0 op_sel_hi:[1,0]
	v_pk_mul_f32 v[12:13], v[152:153], v[120:121]
	v_rcp_f32_e32 v14, v14
	v_rcp_f32_e32 v15, v15
	v_pk_add_f32 v[18:19], v[18:19], 1.0 op_sel_hi:[1,0]
	v_rcp_f32_e32 v18, v18
	v_rcp_f32_e32 v19, v19
	v_pk_mul_f32 v[12:13], v[14:15], v[12:13]
	v_pk_mul_f32 v[14:15], v[150:151], v[118:119]
	v_pk_mul_f32 v[14:15], v[18:19], v[14:15]
	v_exp_f32_e64 v18, -v140
	v_exp_f32_e64 v19, -v141
	v_med3_f32 v7, v12, s13, v250
	v_med3_f32 v12, v13, s13, v250
	v_med3_f32 v13, v10, s13, v250
	v_cvt_pk_fp8_f32 v10, v7, v12
	v_pk_add_f32 v[18:19], v[18:19], 1.0 op_sel_hi:[1,0]
	v_med3_f32 v11, v11, s13, v250
	v_rcp_f32_e32 v18, v18
	v_rcp_f32_e32 v19, v19
	v_cvt_pk_fp8_f32 v10, v13, v11 op_sel:[0,0,1]
	v_med3_f32 v7, v16, s13, v250
	v_med3_f32 v12, v17, s13, v250
	v_pk_mul_f32 v[16:17], v[140:141], v[108:109]
	v_cvt_pk_fp8_f32 v11, v7, v12
	v_pk_mul_f32 v[16:17], v[18:19], v[16:17]
	v_exp_f32_e64 v18, -v146
	v_exp_f32_e64 v19, -v147
	v_med3_f32 v13, v14, s13, v250
	v_med3_f32 v14, v15, s13, v250
	v_cvt_pk_fp8_f32 v11, v13, v14 op_sel:[0,0,1]
	v_pk_add_f32 v[18:19], v[18:19], 1.0 op_sel_hi:[1,0]
	v_rcp_f32_e32 v18, v18
	v_rcp_f32_e32 v19, v19
	global_store_dwordx2 v[182:183], v[10:11], off
	v_lshl_add_u64 v[182:183], v[182:183], 0, v[180:181]
	s_and_b64 vcc, exec, s[8:9]
	s_cbranch_vccz .Lepi_nobar_2
	s_barrier
.Lepi_nobar_2:
	v_pk_mul_f32 v[10:11], v[146:147], v[114:115]
	v_exp_f32_e64 v14, -v144
	v_exp_f32_e64 v15, -v145
	v_pk_mul_f32 v[10:11], v[18:19], v[10:11]
	v_exp_f32_e64 v18, -v142
	v_exp_f32_e64 v19, -v143
	v_pk_add_f32 v[14:15], v[14:15], 1.0 op_sel_hi:[1,0]
	v_pk_mul_f32 v[12:13], v[144:145], v[112:113]
	v_rcp_f32_e32 v14, v14
	v_rcp_f32_e32 v15, v15
	v_pk_add_f32 v[18:19], v[18:19], 1.0 op_sel_hi:[1,0]
	v_rcp_f32_e32 v18, v18
	v_rcp_f32_e32 v19, v19
	v_pk_mul_f32 v[12:13], v[14:15], v[12:13]
	v_pk_mul_f32 v[14:15], v[142:143], v[110:111]
	v_pk_mul_f32 v[14:15], v[18:19], v[14:15]
	v_exp_f32_e64 v18, -v132
	v_exp_f32_e64 v19, -v133
	v_med3_f32 v7, v12, s13, v250
	v_med3_f32 v12, v13, s13, v250
	v_med3_f32 v13, v10, s13, v250
	v_cvt_pk_fp8_f32 v10, v7, v12
	v_pk_add_f32 v[18:19], v[18:19], 1.0 op_sel_hi:[1,0]
	v_med3_f32 v11, v11, s13, v250
	v_rcp_f32_e32 v18, v18
	v_rcp_f32_e32 v19, v19
	v_cvt_pk_fp8_f32 v10, v13, v11 op_sel:[0,0,1]
	v_med3_f32 v7, v16, s13, v250
	v_med3_f32 v12, v17, s13, v250
	v_pk_mul_f32 v[16:17], v[132:133], v[100:101]
	v_cvt_pk_fp8_f32 v11, v7, v12
	v_pk_mul_f32 v[16:17], v[18:19], v[16:17]
	v_exp_f32_e64 v18, -v138
	v_exp_f32_e64 v19, -v139
	v_med3_f32 v13, v14, s13, v250
	v_med3_f32 v14, v15, s13, v250
	v_cvt_pk_fp8_f32 v11, v13, v14 op_sel:[0,0,1]
	v_pk_add_f32 v[18:19], v[18:19], 1.0 op_sel_hi:[1,0]
	v_rcp_f32_e32 v18, v18
	v_rcp_f32_e32 v19, v19
	global_store_dwordx2 v[182:183], v[10:11], off
	v_lshl_add_u64 v[182:183], v[182:183], 0, v[180:181]
	v_pk_mul_f32 v[10:11], v[138:139], v[106:107]
	v_exp_f32_e64 v14, -v136
	v_exp_f32_e64 v15, -v137
	v_pk_mul_f32 v[10:11], v[18:19], v[10:11]
	v_exp_f32_e64 v18, -v134
	v_exp_f32_e64 v19, -v135
	v_pk_add_f32 v[14:15], v[14:15], 1.0 op_sel_hi:[1,0]
	v_pk_mul_f32 v[12:13], v[136:137], v[104:105]
	v_rcp_f32_e32 v14, v14
	v_rcp_f32_e32 v15, v15
	v_pk_add_f32 v[18:19], v[18:19], 1.0 op_sel_hi:[1,0]
	v_rcp_f32_e32 v18, v18
	v_rcp_f32_e32 v19, v19
	v_pk_mul_f32 v[12:13], v[14:15], v[12:13]
	v_pk_mul_f32 v[14:15], v[134:135], v[102:103]
	v_pk_mul_f32 v[14:15], v[18:19], v[14:15]
	v_exp_f32_e64 v18, -v92
	v_exp_f32_e64 v19, -v93
	v_med3_f32 v7, v12, s13, v250
	v_med3_f32 v12, v13, s13, v250
	v_med3_f32 v13, v10, s13, v250
	v_cvt_pk_fp8_f32 v10, v7, v12
	v_pk_add_f32 v[18:19], v[18:19], 1.0 op_sel_hi:[1,0]
	v_med3_f32 v11, v11, s13, v250
	v_rcp_f32_e32 v18, v18
	v_rcp_f32_e32 v19, v19
	v_cvt_pk_fp8_f32 v10, v13, v11 op_sel:[0,0,1]
	v_med3_f32 v7, v16, s13, v250
	v_med3_f32 v12, v17, s13, v250
	v_pk_mul_f32 v[16:17], v[92:93], v[60:61]
	v_cvt_pk_fp8_f32 v11, v7, v12
	v_pk_mul_f32 v[16:17], v[18:19], v[16:17]
	v_exp_f32_e64 v18, -v98
	v_exp_f32_e64 v19, -v99
	v_med3_f32 v13, v14, s13, v250
	v_med3_f32 v14, v15, s13, v250
	v_cvt_pk_fp8_f32 v11, v13, v14 op_sel:[0,0,1]
	v_pk_add_f32 v[18:19], v[18:19], 1.0 op_sel_hi:[1,0]
	v_rcp_f32_e32 v18, v18
	v_rcp_f32_e32 v19, v19
	global_store_dwordx2 v[182:183], v[10:11], off
	v_lshl_add_u64 v[182:183], v[180:181], 2, v[182:183]
	v_lshl_add_u64 v[182:183], v[182:183], 0, v[180:181]
	v_pk_mul_f32 v[10:11], v[98:99], v[66:67]
	v_exp_f32_e64 v14, -v96
	v_exp_f32_e64 v15, -v97
	v_pk_mul_f32 v[10:11], v[18:19], v[10:11]
	v_exp_f32_e64 v18, -v94
	v_exp_f32_e64 v19, -v95
	v_pk_add_f32 v[14:15], v[14:15], 1.0 op_sel_hi:[1,0]
	v_pk_mul_f32 v[12:13], v[96:97], v[64:65]
	v_rcp_f32_e32 v14, v14
	v_rcp_f32_e32 v15, v15
	v_pk_add_f32 v[18:19], v[18:19], 1.0 op_sel_hi:[1,0]
	v_rcp_f32_e32 v18, v18
	v_rcp_f32_e32 v19, v19
	v_pk_mul_f32 v[12:13], v[14:15], v[12:13]
	v_pk_mul_f32 v[14:15], v[94:95], v[62:63]
	v_pk_mul_f32 v[14:15], v[18:19], v[14:15]
	v_exp_f32_e64 v18, -v84
	v_exp_f32_e64 v19, -v85
	v_med3_f32 v7, v12, s13, v250
	v_med3_f32 v12, v13, s13, v250
	v_med3_f32 v13, v10, s13, v250
	v_cvt_pk_fp8_f32 v10, v7, v12
	v_pk_add_f32 v[18:19], v[18:19], 1.0 op_sel_hi:[1,0]
	v_med3_f32 v11, v11, s13, v250
	v_rcp_f32_e32 v18, v18
	v_rcp_f32_e32 v19, v19
	v_cvt_pk_fp8_f32 v10, v13, v11 op_sel:[0,0,1]
	v_med3_f32 v7, v16, s13, v250
	v_med3_f32 v12, v17, s13, v250
	v_pk_mul_f32 v[16:17], v[84:85], v[52:53]
	v_cvt_pk_fp8_f32 v11, v7, v12
	v_pk_mul_f32 v[16:17], v[18:19], v[16:17]
	v_exp_f32_e64 v18, -v90
	v_exp_f32_e64 v19, -v91
	v_med3_f32 v13, v14, s13, v250
	v_med3_f32 v14, v15, s13, v250
	v_cvt_pk_fp8_f32 v11, v13, v14 op_sel:[0,0,1]
	v_pk_add_f32 v[18:19], v[18:19], 1.0 op_sel_hi:[1,0]
	v_rcp_f32_e32 v18, v18
	v_rcp_f32_e32 v19, v19
	v_exp_f32_e64 v14, -v88
	v_exp_f32_e64 v15, -v89
	global_store_dwordx2 v[182:183], v[10:11], off
	v_lshl_add_u64 v[182:183], v[182:183], 0, v[180:181]
	v_pk_mul_f32 v[10:11], v[90:91], v[58:59]
	v_pk_mul_f32 v[12:13], v[88:89], v[56:57]
	v_pk_mul_f32 v[10:11], v[18:19], v[10:11]
	v_exp_f32_e64 v18, -v86
	v_exp_f32_e64 v19, -v87
	v_pk_add_f32 v[14:15], v[14:15], 1.0 op_sel_hi:[1,0]
	v_rcp_f32_e32 v14, v14
	v_rcp_f32_e32 v15, v15
	v_pk_add_f32 v[18:19], v[18:19], 1.0 op_sel_hi:[1,0]
	v_rcp_f32_e32 v18, v18
	v_rcp_f32_e32 v19, v19
	v_pk_mul_f32 v[12:13], v[14:15], v[12:13]
	v_pk_mul_f32 v[14:15], v[86:87], v[54:55]
	v_med3_f32 v7, v12, s13, v250
	v_med3_f32 v12, v13, s13, v250
	v_med3_f32 v13, v10, s13, v250
	v_pk_mul_f32 v[14:15], v[18:19], v[14:15]
	v_cvt_pk_fp8_f32 v10, v7, v12
	v_exp_f32_e64 v18, -v76
	v_exp_f32_e64 v19, -v77
	v_med3_f32 v11, v11, s13, v250
	v_cvt_pk_fp8_f32 v10, v13, v11 op_sel:[0,0,1]
	v_med3_f32 v7, v16, s13, v250
	v_med3_f32 v12, v17, s13, v250
	v_pk_add_f32 v[18:19], v[18:19], 1.0 op_sel_hi:[1,0]
	v_cvt_pk_fp8_f32 v11, v7, v12
	v_rcp_f32_e32 v18, v18
	v_rcp_f32_e32 v19, v19
	v_med3_f32 v13, v14, s13, v250
	v_med3_f32 v14, v15, s13, v250
	v_pk_mul_f32 v[16:17], v[76:77], v[44:45]
	v_cvt_pk_fp8_f32 v11, v13, v14 op_sel:[0,0,1]
	v_exp_f32_e64 v14, -v80
	v_exp_f32_e64 v15, -v81
	v_pk_mul_f32 v[16:17], v[18:19], v[16:17]
	v_exp_f32_e64 v18, -v82
	v_exp_f32_e64 v19, -v83
	v_pk_add_f32 v[14:15], v[14:15], 1.0 op_sel_hi:[1,0]
	v_rcp_f32_e32 v14, v14
	v_pk_add_f32 v[18:19], v[18:19], 1.0 op_sel_hi:[1,0]
	v_rcp_f32_e32 v15, v15
	v_rcp_f32_e32 v18, v18
	v_rcp_f32_e32 v19, v19
	global_store_dwordx2 v[182:183], v[10:11], off
	v_lshl_add_u64 v[182:183], v[182:183], 0, v[180:181]
	v_pk_mul_f32 v[10:11], v[82:83], v[50:51]
	v_pk_mul_f32 v[12:13], v[80:81], v[48:49]
	v_pk_mul_f32 v[12:13], v[14:15], v[12:13]
	v_pk_mul_f32 v[10:11], v[18:19], v[10:11]
	v_exp_f32_e64 v18, -v78
	v_exp_f32_e64 v19, -v79
	v_med3_f32 v7, v12, s13, v250
	v_med3_f32 v12, v13, s13, v250
	v_med3_f32 v13, v10, s13, v250
	v_cvt_pk_fp8_f32 v10, v7, v12
	v_pk_add_f32 v[18:19], v[18:19], 1.0 op_sel_hi:[1,0]
	v_med3_f32 v11, v11, s13, v250
	v_rcp_f32_e32 v18, v18
	v_rcp_f32_e32 v19, v19
	v_cvt_pk_fp8_f32 v10, v13, v11 op_sel:[0,0,1]
	v_med3_f32 v7, v16, s13, v250
	v_med3_f32 v12, v17, s13, v250
	v_cvt_pk_fp8_f32 v11, v7, v12
	v_pk_mul_f32 v[14:15], v[78:79], v[46:47]
	v_pk_mul_f32 v[14:15], v[18:19], v[14:15]
	v_med3_f32 v13, v14, s13, v250
	v_med3_f32 v14, v15, s13, v250
	v_cvt_pk_fp8_f32 v11, v13, v14 op_sel:[0,0,1]
	v_exp_f32_e64 v14, -v68
	v_exp_f32_e64 v15, -v69
	v_pk_mul_f32 v[12:13], v[68:69], v[36:37]
	global_store_dwordx2 v[182:183], v[10:11], off
	v_lshl_add_u64 v[182:183], v[182:183], 0, v[180:181]
	v_exp_f32_e64 v10, -v72
	v_pk_add_f32 v[14:15], v[14:15], 1.0 op_sel_hi:[1,0]
	v_exp_f32_e64 v11, -v73
	v_rcp_f32_e32 v14, v14
	v_rcp_f32_e32 v15, v15
	v_pk_add_f32 v[10:11], v[10:11], 1.0 op_sel_hi:[1,0]
	v_pk_mul_f32 v[12:13], v[14:15], v[12:13]
	v_exp_f32_e64 v14, -v74
	v_exp_f32_e64 v15, -v75
	v_rcp_f32_e32 v10, v10
	v_rcp_f32_e32 v11, v11
	v_pk_mul_f32 v[6:7], v[74:75], v[42:43]
	v_pk_add_f32 v[14:15], v[14:15], 1.0 op_sel_hi:[1,0]
	v_pk_mul_f32 v[8:9], v[72:73], v[40:41]
	v_rcp_f32_e32 v14, v14
	v_rcp_f32_e32 v15, v15
	v_pk_mul_f32 v[8:9], v[10:11], v[8:9]
	v_med3_f32 v5, v8, s13, v250
	v_pk_mul_f32 v[6:7], v[14:15], v[6:7]
	v_exp_f32_e64 v14, -v70
	v_exp_f32_e64 v15, -v71
	v_med3_f32 v8, v9, s13, v250
	v_cvt_pk_fp8_f32 v4, v5, v8
	v_pk_add_f32 v[14:15], v[14:15], 1.0 op_sel_hi:[1,0]
	v_med3_f32 v6, v6, s13, v250
	v_rcp_f32_e32 v14, v14
	v_rcp_f32_e32 v15, v15
	v_med3_f32 v7, v7, s13, v250
	v_cvt_pk_fp8_f32 v4, v6, v7 op_sel:[0,0,1]
	v_med3_f32 v6, v12, s13, v250
	v_med3_f32 v7, v13, s13, v250
	v_cvt_pk_fp8_f32 v5, v6, v7
	v_pk_mul_f32 v[10:11], v[70:71], v[38:39]
	s_mov_b64 s[22:23], -1
	v_pk_mul_f32 v[10:11], v[14:15], v[10:11]
	s_andn2_b64 vcc, exec, s[4:5]
	v_med3_f32 v8, v10, s13, v250
	v_med3_f32 v9, v11, s13, v250
	v_cvt_pk_fp8_f32 v5, v8, v9 op_sel:[0,0,1]
	s_mov_b32 s58, 0x19b00000
	v_readlane_b32 s59, v255, 10
	s_mov_b32 s60, 0xff61b1e6
	s_mov_b32 s56, 0x3a800000
	s_mov_b64 s[62:63], 0x800
	s_mov_b32 s64, 0x3b000000
	global_store_dwordx2 v[182:183], v[4:5], off
	s_cbranch_vccnz .LBB0_1083
	s_andn2_b64 vcc, exec, s[6:7]
	s_cbranch_vccnz .LBB0_1082
	s_barrier
	s_branch .LBB0_1082
